# P18 dispatch: 256-workgroup expert-count reduction done as a 64-lane parallel sum (32 loads in flight) instead of a 128-iteration load/wait loop on 8 lanes
# speedup vs baseline: 1.0223x; 1.0105x over previous
; __global__ void __launch_bounds__(NTHREADS, 2) fwd_kernel(Args args) {
;     ...
;         if (tid < NE) { int before = 0, total = 0; for (int bb = 0; bb < G; ++bb) { const int c = CNT[bb * NE + tid]; total += c; before += (bb < bx) ? c : 0; } sh[tid] = before; sh[16 + tid] = total; }
.LBB0_1243:
	s_or_b64 exec, exec, s[4:5]
	v_mov_b32_e32 v2, v0
	s_waitcnt lgkmcnt(0)
	s_barrier
	s_nop 0
	s_cmpk_eq_i32 s76, 0x100
	s_cbranch_scc0 .Lp18_orig
	v_cmp_gt_i32_e32 vcc, 64, v2
	s_and_saveexec_b64 s[8:9], vcc
	s_cbranch_execz .LBB0_1254
	v_and_b32_e32 v90, 7, v2
	v_lshrrev_b32_e32 v91, 3, v2
	v_lshlrev_b32_e32 v92, 10, v91
	v_lshl_add_u32 v92, v90, 2, v92
	s_add_u32 s4, s70, 0x110000
	s_addc_u32 s5, s71, 0
	global_load_dword v100, v92, s[4:5] offset:0
	global_load_dword v101, v92, s[4:5] offset:32
	global_load_dword v102, v92, s[4:5] offset:64
	global_load_dword v103, v92, s[4:5] offset:96
	global_load_dword v104, v92, s[4:5] offset:128
	global_load_dword v105, v92, s[4:5] offset:160
	global_load_dword v106, v92, s[4:5] offset:192
	global_load_dword v107, v92, s[4:5] offset:224
	global_load_dword v108, v92, s[4:5] offset:256
	global_load_dword v109, v92, s[4:5] offset:288
	global_load_dword v110, v92, s[4:5] offset:320
	global_load_dword v111, v92, s[4:5] offset:352
	global_load_dword v112, v92, s[4:5] offset:384
	global_load_dword v113, v92, s[4:5] offset:416
	global_load_dword v114, v92, s[4:5] offset:448
	global_load_dword v115, v92, s[4:5] offset:480
	global_load_dword v116, v92, s[4:5] offset:512
	global_load_dword v117, v92, s[4:5] offset:544
	global_load_dword v118, v92, s[4:5] offset:576
	global_load_dword v119, v92, s[4:5] offset:608
	global_load_dword v120, v92, s[4:5] offset:640
	global_load_dword v121, v92, s[4:5] offset:672
	global_load_dword v122, v92, s[4:5] offset:704
	global_load_dword v123, v92, s[4:5] offset:736
	global_load_dword v124, v92, s[4:5] offset:768
	global_load_dword v125, v92, s[4:5] offset:800
	global_load_dword v126, v92, s[4:5] offset:832
	global_load_dword v127, v92, s[4:5] offset:864
	global_load_dword v128, v92, s[4:5] offset:896
	global_load_dword v129, v92, s[4:5] offset:928
	global_load_dword v130, v92, s[4:5] offset:960
	global_load_dword v131, v92, s[4:5] offset:992
	v_lshlrev_b32_e32 v93, 5, v91
	v_sub_u32_e32 v93, s2, v93
	v_mov_b32_e32 v94, 0
	v_mov_b32_e32 v95, 0
	s_waitcnt vmcnt(0)
; __global__ void __launch_bounds__(NTHREADS, 2) fwd_kernel(Args args) {
;     ...
;         if (tid < NE) { int before = 0, total = 0; for (int bb = 0; bb < G; ++bb) { const int c = CNT[bb * NE + tid]; total += c; before += (bb < bx) ? c : 0; } sh[tid] = before; sh[16 + tid] = total; }
	v_cmp_lt_i32_e32 vcc, 0, v93
	v_add_u32_e32 v94, v94, v100
	s_nop 0
	v_cndmask_b32_e32 v96, 0, v100, vcc
	v_add_u32_e32 v95, v95, v96
	v_cmp_lt_i32_e32 vcc, 1, v93
	v_add_u32_e32 v94, v94, v101
	s_nop 0
	v_cndmask_b32_e32 v96, 0, v101, vcc
	v_add_u32_e32 v95, v95, v96
	v_cmp_lt_i32_e32 vcc, 2, v93
	v_add_u32_e32 v94, v94, v102
	s_nop 0
	v_cndmask_b32_e32 v96, 0, v102, vcc
	v_add_u32_e32 v95, v95, v96
	v_cmp_lt_i32_e32 vcc, 3, v93
	v_add_u32_e32 v94, v94, v103
	s_nop 0
	v_cndmask_b32_e32 v96, 0, v103, vcc
	v_add_u32_e32 v95, v95, v96
	v_cmp_lt_i32_e32 vcc, 4, v93
	v_add_u32_e32 v94, v94, v104
	s_nop 0
	v_cndmask_b32_e32 v96, 0, v104, vcc
	v_add_u32_e32 v95, v95, v96
	v_cmp_lt_i32_e32 vcc, 5, v93
	v_add_u32_e32 v94, v94, v105
	s_nop 0
	v_cndmask_b32_e32 v96, 0, v105, vcc
	v_add_u32_e32 v95, v95, v96
	v_cmp_lt_i32_e32 vcc, 6, v93
	v_add_u32_e32 v94, v94, v106
	s_nop 0
	v_cndmask_b32_e32 v96, 0, v106, vcc
	v_add_u32_e32 v95, v95, v96
	v_cmp_lt_i32_e32 vcc, 7, v93
	v_add_u32_e32 v94, v94, v107
	s_nop 0
	v_cndmask_b32_e32 v96, 0, v107, vcc
	v_add_u32_e32 v95, v95, v96
	v_cmp_lt_i32_e32 vcc, 8, v93
	v_add_u32_e32 v94, v94, v108
	s_nop 0
	v_cndmask_b32_e32 v96, 0, v108, vcc
	v_add_u32_e32 v95, v95, v96
	v_cmp_lt_i32_e32 vcc, 9, v93
	v_add_u32_e32 v94, v94, v109
	s_nop 0
	v_cndmask_b32_e32 v96, 0, v109, vcc
	v_add_u32_e32 v95, v95, v96
	v_cmp_lt_i32_e32 vcc, 10, v93
	v_add_u32_e32 v94, v94, v110
	s_nop 0
	v_cndmask_b32_e32 v96, 0, v110, vcc
	v_add_u32_e32 v95, v95, v96
	v_cmp_lt_i32_e32 vcc, 11, v93
	v_add_u32_e32 v94, v94, v111
	s_nop 0
	v_cndmask_b32_e32 v96, 0, v111, vcc
	v_add_u32_e32 v95, v95, v96
	v_cmp_lt_i32_e32 vcc, 12, v93
	v_add_u32_e32 v94, v94, v112
	s_nop 0
	v_cndmask_b32_e32 v96, 0, v112, vcc
	v_add_u32_e32 v95, v95, v96
	v_cmp_lt_i32_e32 vcc, 13, v93
	v_add_u32_e32 v94, v94, v113
	s_nop 0
	v_cndmask_b32_e32 v96, 0, v113, vcc
	v_add_u32_e32 v95, v95, v96
	v_cmp_lt_i32_e32 vcc, 14, v93
	v_add_u32_e32 v94, v94, v114
	s_nop 0
	v_cndmask_b32_e32 v96, 0, v114, vcc
	v_add_u32_e32 v95, v95, v96
	v_cmp_lt_i32_e32 vcc, 15, v93
	v_add_u32_e32 v94, v94, v115
	s_nop 0
	v_cndmask_b32_e32 v96, 0, v115, vcc
	v_add_u32_e32 v95, v95, v96
	v_cmp_lt_i32_e32 vcc, 16, v93
	v_add_u32_e32 v94, v94, v116
	s_nop 0
	v_cndmask_b32_e32 v96, 0, v116, vcc
	v_add_u32_e32 v95, v95, v96
	v_cmp_lt_i32_e32 vcc, 17, v93
	v_add_u32_e32 v94, v94, v117
	s_nop 0
	v_cndmask_b32_e32 v96, 0, v117, vcc
	v_add_u32_e32 v95, v95, v96
	v_cmp_lt_i32_e32 vcc, 18, v93
	v_add_u32_e32 v94, v94, v118
	s_nop 0
	v_cndmask_b32_e32 v96, 0, v118, vcc
	v_add_u32_e32 v95, v95, v96
	v_cmp_lt_i32_e32 vcc, 19, v93
	v_add_u32_e32 v94, v94, v119
	s_nop 0
	v_cndmask_b32_e32 v96, 0, v119, vcc
	v_add_u32_e32 v95, v95, v96
	v_cmp_lt_i32_e32 vcc, 20, v93
	v_add_u32_e32 v94, v94, v120
	s_nop 0
	v_cndmask_b32_e32 v96, 0, v120, vcc
	v_add_u32_e32 v95, v95, v96
	v_cmp_lt_i32_e32 vcc, 21, v93
	v_add_u32_e32 v94, v94, v121
	s_nop 0
	v_cndmask_b32_e32 v96, 0, v121, vcc
	v_add_u32_e32 v95, v95, v96
	v_cmp_lt_i32_e32 vcc, 22, v93
	v_add_u32_e32 v94, v94, v122
	s_nop 0
	v_cndmask_b32_e32 v96, 0, v122, vcc
	v_add_u32_e32 v95, v95, v96
	v_cmp_lt_i32_e32 vcc, 23, v93
	v_add_u32_e32 v94, v94, v123
	s_nop 0
	v_cndmask_b32_e32 v96, 0, v123, vcc
	v_add_u32_e32 v95, v95, v96
	v_cmp_lt_i32_e32 vcc, 24, v93
	v_add_u32_e32 v94, v94, v124
	s_nop 0
	v_cndmask_b32_e32 v96, 0, v124, vcc
	v_add_u32_e32 v95, v95, v96
	v_cmp_lt_i32_e32 vcc, 25, v93
	v_add_u32_e32 v94, v94, v125
	s_nop 0
	v_cndmask_b32_e32 v96, 0, v125, vcc
	v_add_u32_e32 v95, v95, v96
	v_cmp_lt_i32_e32 vcc, 26, v93
	v_add_u32_e32 v94, v94, v126
	s_nop 0
	v_cndmask_b32_e32 v96, 0, v126, vcc
	v_add_u32_e32 v95, v95, v96
	v_cmp_lt_i32_e32 vcc, 27, v93
	v_add_u32_e32 v94, v94, v127
	s_nop 0
	v_cndmask_b32_e32 v96, 0, v127, vcc
	v_add_u32_e32 v95, v95, v96
	v_cmp_lt_i32_e32 vcc, 28, v93
	v_add_u32_e32 v94, v94, v128
	s_nop 0
	v_cndmask_b32_e32 v96, 0, v128, vcc
	v_add_u32_e32 v95, v95, v96
	v_cmp_lt_i32_e32 vcc, 29, v93
	v_add_u32_e32 v94, v94, v129
	s_nop 0
	v_cndmask_b32_e32 v96, 0, v129, vcc
	v_add_u32_e32 v95, v95, v96
	v_cmp_lt_i32_e32 vcc, 30, v93
	v_add_u32_e32 v94, v94, v130
	s_nop 0
	v_cndmask_b32_e32 v96, 0, v130, vcc
	v_add_u32_e32 v95, v95, v96
	v_cmp_lt_i32_e32 vcc, 31, v93
	v_add_u32_e32 v94, v94, v131
	s_nop 0
	v_cndmask_b32_e32 v96, 0, v131, vcc
	v_add_u32_e32 v95, v95, v96
	v_lshlrev_b32_e32 v97, 2, v2
	v_add_u32_e32 v97, 0x1000, v97
	ds_write_b32 v97, v94
	ds_write_b32 v97, v95 offset:256
	v_lshlrev_b32_e32 v98, 2, v90
	v_add_u32_e32 v98, 0x1000, v98
	s_waitcnt lgkmcnt(0)
	ds_read_b32 v132, v98 offset:0
	ds_read_b32 v133, v98 offset:32
	ds_read_b32 v134, v98 offset:64
	ds_read_b32 v135, v98 offset:96
	ds_read_b32 v136, v98 offset:128
	ds_read_b32 v137, v98 offset:160
	ds_read_b32 v138, v98 offset:192
	ds_read_b32 v139, v98 offset:224
	ds_read_b32 v140, v98 offset:256
	ds_read_b32 v141, v98 offset:288
	ds_read_b32 v142, v98 offset:320
	ds_read_b32 v143, v98 offset:352
	ds_read_b32 v144, v98 offset:384
	ds_read_b32 v145, v98 offset:416
	ds_read_b32 v146, v98 offset:448
	ds_read_b32 v147, v98 offset:480
	s_waitcnt lgkmcnt(0)
	v_cmp_gt_i32_e32 vcc, 8, v2
	s_and_b64 exec, exec, vcc
	v_add_u32_e32 v1, v132, v133
	v_add_u32_e32 v1, v1, v134
	v_add_u32_e32 v1, v1, v135
	v_add_u32_e32 v1, v1, v136
	v_add_u32_e32 v1, v1, v137
	v_add_u32_e32 v1, v1, v138
	v_add_u32_e32 v1, v1, v139
	v_add_u32_e32 v6, v140, v141
	v_add_u32_e32 v6, v6, v142
	v_add_u32_e32 v6, v6, v143
	v_add_u32_e32 v6, v6, v144
	v_add_u32_e32 v6, v6, v145
	v_add_u32_e32 v6, v6, v146
	v_add_u32_e32 v6, v6, v147
	v_lshl_add_u32 v3, v2, 2, 0
	ds_write2_b32 v3, v6, v1 offset1:16
	s_branch .LBB0_1254
.Lp18_orig:
	v_cmp_gt_i32_e32 vcc, 8, v2
	s_and_saveexec_b64 s[8:9], vcc
	s_cbranch_execz .LBB0_1254
	s_cmp_lt_i32 s76, 1
	s_cbranch_scc1 .LBB0_1249
	s_cmp_eq_u32 s76, 1
	s_cbranch_scc1 .LBB0_1250
	s_and_b32 s10, s76, 0x7ffffffe
	v_mov_b32_e32 v1, v2
	s_mov_b32 s11, s2
	s_mov_b32 s12, s2
	s_mov_b32 s13, 1
	v_mov_b32_e32 v3, 0
	s_mov_b32 s14, 0
	s_mov_b32 s15, s10
	v_mov_b32_e32 v4, 0
	v_mov_b32_e32 v5, 0
	v_mov_b32_e32 v7, 0
